# nt hints plus FFUP GEMM K-loop LDS-DMA issue rebalanced 4+4 per sub-phase (was 2+6), waits re-derived
# speedup vs baseline: 1.0063x; 1.0050x over previous
.LBB0_758:
	ds_read_b128 v[146:149], v152
	ds_read_b128 v[156:159], v152 offset:1024
	ds_read_b128 v[160:163], v152 offset:2048
	ds_read_b128 v[164:167], v152 offset:3072
	ds_read_b128 v[168:171], v153
	ds_read_b128 v[172:175], v153 offset:1024
	ds_read_b128 v[176:179], v153 offset:2048
	ds_read_b128 v[180:183], v153 offset:3072
	s_add_u32 s28, s26, 0xfff80080
	s_addc_u32 s29, s27, -1
	s_cmp_eq_u32 s61, 28
	s_cselect_b32 s31, s19, s29
	s_cselect_b32 s30, s49, s28
	s_cselect_b32 s29, s17, s60
	s_cselect_b32 s28, s50, s51
	v_lshl_add_u64 v[184:185], s[26:27], 0, v[138:139]
	s_add_i32 m0, s25, 0xc000
	ds_read_b128 v[188:191], v154
	ds_read_b128 v[192:195], v154 offset:1024
	ds_read_b128 v[196:199], v154 offset:2048
	ds_read_b128 v[200:203], v154 offset:3072
	ds_read_b128 v[204:207], v154 offset:4096
	ds_read_b128 v[208:211], v154 offset:5120
	ds_read_b128 v[212:215], v154 offset:6144
	ds_read_b128 v[216:219], v154 offset:7168
	global_load_lds_dwordx4 v[184:185], off
	v_lshl_add_u64 v[184:185], s[26:27], 0, v[140:141]
	s_add_i32 m0, s25, 0xe000
	s_nop 0
	global_load_lds_dwordx4 v[184:185], off
	s_add_u32 s98, s51, 0x7ff80
	s_addc_u32 s99, s60, 0
	s_add_i32 s100, s34, 0x1c000
	v_lshl_add_u64 v[184:185], s[98:99], 0, v[134:135]
	s_mov_b32 m0, s100
	s_nop 0
	global_load_lds_dwordx4 v[184:185], off
	v_lshl_add_u64 v[184:185], s[98:99], 0, v[130:131]
	s_add_i32 m0, s100, 0x2000
	s_nop 0
	global_load_lds_dwordx4 v[184:185], off
	s_waitcnt vmcnt(8)
	s_waitcnt lgkmcnt(0)
	s_barrier
	s_setprio 1
	s_waitcnt lgkmcnt(0)
	v_mfma_f32_16x16x32_f16 v[126:129], v[146:149], v[188:191], v[126:129]
	v_mfma_f32_16x16x32_f16 v[122:125], v[160:163], v[188:191], v[122:125]
	v_mfma_f32_16x16x32_f16 v[110:113], v[146:149], v[196:199], v[110:113]
	v_mfma_f32_16x16x32_f16 v[106:109], v[160:163], v[196:199], v[106:109]
	v_mfma_f32_16x16x32_f16 v[94:97], v[146:149], v[204:207], v[94:97]
	v_mfma_f32_16x16x32_f16 v[90:93], v[160:163], v[204:207], v[90:93]
	v_mfma_f32_16x16x32_f16 v[78:81], v[146:149], v[212:215], v[78:81]
	v_mfma_f32_16x16x32_f16 v[74:77], v[160:163], v[212:215], v[74:77]
	v_mfma_f32_16x16x32_f16 v[126:129], v[156:159], v[192:195], v[126:129]
	v_mfma_f32_16x16x32_f16 v[122:125], v[164:167], v[192:195], v[122:125]
	v_mfma_f32_16x16x32_f16 v[110:113], v[156:159], v[200:203], v[110:113]
	v_mfma_f32_16x16x32_f16 v[106:109], v[164:167], v[200:203], v[106:109]
	v_mfma_f32_16x16x32_f16 v[94:97], v[156:159], v[208:211], v[94:97]
	v_mfma_f32_16x16x32_f16 v[90:93], v[164:167], v[208:211], v[90:93]
	v_mfma_f32_16x16x32_f16 v[78:81], v[156:159], v[216:219], v[78:81]
	v_mfma_f32_16x16x32_f16 v[74:77], v[164:167], v[216:219], v[74:77]
	s_setprio 0
	s_setprio 1
	v_mfma_f32_16x16x32_f16 v[118:121], v[168:171], v[188:191], v[118:121]
	v_mfma_f32_16x16x32_f16 v[114:117], v[176:179], v[188:191], v[114:117]
	v_mfma_f32_16x16x32_f16 v[102:105], v[168:171], v[196:199], v[102:105]
	v_mfma_f32_16x16x32_f16 v[98:101], v[176:179], v[196:199], v[98:101]
	v_mfma_f32_16x16x32_f16 v[86:89], v[168:171], v[204:207], v[86:89]
	v_mfma_f32_16x16x32_f16 v[82:85], v[176:179], v[204:207], v[82:85]
	v_mfma_f32_16x16x32_f16 v[70:73], v[168:171], v[212:215], v[70:73]
	v_mfma_f32_16x16x32_f16 v[66:69], v[176:179], v[212:215], v[66:69]
	v_mfma_f32_16x16x32_f16 v[118:121], v[172:175], v[192:195], v[118:121]
	v_mfma_f32_16x16x32_f16 v[114:117], v[180:183], v[192:195], v[114:117]
	v_mfma_f32_16x16x32_f16 v[102:105], v[172:175], v[200:203], v[102:105]
	v_mfma_f32_16x16x32_f16 v[98:101], v[180:183], v[200:203], v[98:101]
	v_mfma_f32_16x16x32_f16 v[86:89], v[172:175], v[208:211], v[86:89]
	v_mfma_f32_16x16x32_f16 v[82:85], v[180:183], v[208:211], v[82:85]
	v_mfma_f32_16x16x32_f16 v[70:73], v[172:175], v[216:219], v[70:73]
	v_mfma_f32_16x16x32_f16 v[66:69], v[180:183], v[216:219], v[66:69]
	s_setprio 0
	s_barrier
	s_add_i32 s62, s44, s34
	v_lshl_add_u64 v[184:185], s[28:29], 0, v[134:135]
	s_mov_b32 m0, s62
	ds_read_b128 v[188:191], v154 offset:16384
	ds_read_b128 v[192:195], v154 offset:17408
	ds_read_b128 v[196:199], v154 offset:18432
	ds_read_b128 v[200:203], v154 offset:19456
	ds_read_b128 v[204:207], v154 offset:20480
	ds_read_b128 v[208:211], v154 offset:21504
	ds_read_b128 v[212:215], v154 offset:22528
	ds_read_b128 v[216:219], v154 offset:23552
	global_load_lds_dwordx4 v[184:185], off
	s_add_i32 m0, s62, 0x2000
	v_lshl_add_u64 v[220:221], s[28:29], 0, v[130:131]
	global_load_lds_dwordx4 v[220:221], off
	v_lshl_add_u64 v[224:225], s[30:31], 0, v[132:133]
	v_lshl_add_u64 v[222:223], s[30:31], 0, v[136:137]
	s_mov_b32 m0, s25
	s_nop 0
	global_load_lds_dwordx4 v[222:223], off
	s_mov_b32 m0, s37
	s_nop 0
	global_load_lds_dwordx4 v[224:225], off
	s_waitcnt vmcnt(4)
	s_waitcnt lgkmcnt(0)
	s_barrier
	s_setprio 1
	s_waitcnt lgkmcnt(0)
	v_mfma_f32_16x16x32_f16 v[62:65], v[146:149], v[188:191], v[62:65]
	v_mfma_f32_16x16x32_f16 v[58:61], v[160:163], v[188:191], v[58:61]
	v_mfma_f32_16x16x32_f16 v[46:49], v[146:149], v[196:199], v[46:49]
	v_mfma_f32_16x16x32_f16 v[42:45], v[160:163], v[196:199], v[42:45]
	v_mfma_f32_16x16x32_f16 v[30:33], v[146:149], v[204:207], v[30:33]
	v_mfma_f32_16x16x32_f16 v[26:29], v[160:163], v[204:207], v[26:29]
	v_mfma_f32_16x16x32_f16 v[14:17], v[146:149], v[212:215], v[14:17]
	v_mfma_f32_16x16x32_f16 v[10:13], v[160:163], v[212:215], v[10:13]
	v_mfma_f32_16x16x32_f16 v[62:65], v[156:159], v[192:195], v[62:65]
	v_mfma_f32_16x16x32_f16 v[58:61], v[164:167], v[192:195], v[58:61]
	v_mfma_f32_16x16x32_f16 v[46:49], v[156:159], v[200:203], v[46:49]
	v_mfma_f32_16x16x32_f16 v[42:45], v[164:167], v[200:203], v[42:45]
	v_mfma_f32_16x16x32_f16 v[30:33], v[156:159], v[208:211], v[30:33]
	v_mfma_f32_16x16x32_f16 v[26:29], v[164:167], v[208:211], v[26:29]
	v_mfma_f32_16x16x32_f16 v[14:17], v[156:159], v[216:219], v[14:17]
	v_mfma_f32_16x16x32_f16 v[10:13], v[164:167], v[216:219], v[10:13]
	s_setprio 0
	s_setprio 1
	v_mfma_f32_16x16x32_f16 v[54:57], v[168:171], v[188:191], v[54:57]
	v_mfma_f32_16x16x32_f16 v[50:53], v[176:179], v[188:191], v[50:53]
	v_mfma_f32_16x16x32_f16 v[38:41], v[168:171], v[196:199], v[38:41]
	v_mfma_f32_16x16x32_f16 v[34:37], v[176:179], v[196:199], v[34:37]
	v_mfma_f32_16x16x32_f16 v[22:25], v[168:171], v[204:207], v[22:25]
	v_mfma_f32_16x16x32_f16 v[18:21], v[176:179], v[204:207], v[18:21]
	v_mfma_f32_16x16x32_f16 v[6:9], v[168:171], v[212:215], v[6:9]
	v_mfma_f32_16x16x32_f16 v[2:5], v[176:179], v[212:215], v[2:5]
	v_mfma_f32_16x16x32_f16 v[54:57], v[172:175], v[192:195], v[54:57]
	v_mfma_f32_16x16x32_f16 v[50:53], v[180:183], v[192:195], v[50:53]
	v_mfma_f32_16x16x32_f16 v[38:41], v[172:175], v[200:203], v[38:41]
	v_mfma_f32_16x16x32_f16 v[34:37], v[180:183], v[200:203], v[34:37]
	v_mfma_f32_16x16x32_f16 v[22:25], v[172:175], v[208:211], v[22:25]
	v_mfma_f32_16x16x32_f16 v[18:21], v[180:183], v[208:211], v[18:21]
	v_mfma_f32_16x16x32_f16 v[6:9], v[172:175], v[216:219], v[6:9]
	v_mfma_f32_16x16x32_f16 v[2:5], v[180:183], v[216:219], v[2:5]
	s_setprio 0
	s_barrier
	s_add_i32 s62, 0, 0x18000
	s_add_i32 s63, 0, 0x1c000
	v_add_u32_e32 v164, s62, v150
	v_add_u32_e32 v180, s63, v150
	ds_read_b128 v[146:149], v164
	ds_read_b128 v[156:159], v164 offset:1024
	ds_read_b128 v[160:163], v164 offset:2048
	ds_read_b128 v[164:167], v164 offset:3072
	ds_read_b128 v[168:171], v180
	ds_read_b128 v[172:175], v180 offset:1024
	ds_read_b128 v[176:179], v180 offset:2048
	ds_read_b128 v[180:183], v180 offset:3072
	s_add_u32 s30, s30, 0x80000
	s_addc_u32 s31, s31, 0
	s_mov_b32 m0, s38
	v_lshl_add_u64 v[226:227], s[30:31], 0, v[136:137]
	ds_read_b128 v[188:191], v154 offset:32768
	ds_read_b128 v[192:195], v154 offset:33792
	ds_read_b128 v[196:199], v154 offset:34816
	ds_read_b128 v[200:203], v154 offset:35840
	ds_read_b128 v[204:207], v154 offset:36864
	ds_read_b128 v[208:211], v154 offset:37888
	ds_read_b128 v[212:215], v154 offset:38912
	ds_read_b128 v[216:219], v154 offset:39936
	global_load_lds_dwordx4 v[226:227], off
	v_lshl_add_u64 v[226:227], s[30:31], 0, v[132:133]
	s_mov_b32 m0, s39
	s_nop 0
	global_load_lds_dwordx4 v[226:227], off
	s_add_u32 s98, s28, 0x80000
	s_addc_u32 s99, s29, 0
	s_add_i32 s100, s45, s34
	v_lshl_add_u64 v[226:227], s[98:99], 0, v[134:135]
	s_mov_b32 m0, s100
	s_nop 0
	global_load_lds_dwordx4 v[226:227], off
	v_lshl_add_u64 v[226:227], s[98:99], 0, v[130:131]
	s_add_i32 m0, s100, 0x2000
	s_nop 0
	global_load_lds_dwordx4 v[226:227], off
	s_waitcnt vmcnt(8)
	s_waitcnt lgkmcnt(0)
	s_barrier
	s_setprio 1
	s_waitcnt lgkmcnt(0)
	v_mfma_f32_16x16x32_f16 v[126:129], v[146:149], v[188:191], v[126:129]
	v_mfma_f32_16x16x32_f16 v[122:125], v[160:163], v[188:191], v[122:125]
	v_mfma_f32_16x16x32_f16 v[110:113], v[146:149], v[196:199], v[110:113]
	v_mfma_f32_16x16x32_f16 v[106:109], v[160:163], v[196:199], v[106:109]
	v_mfma_f32_16x16x32_f16 v[94:97], v[146:149], v[204:207], v[94:97]
	v_mfma_f32_16x16x32_f16 v[90:93], v[160:163], v[204:207], v[90:93]
	v_mfma_f32_16x16x32_f16 v[78:81], v[146:149], v[212:215], v[78:81]
	v_mfma_f32_16x16x32_f16 v[74:77], v[160:163], v[212:215], v[74:77]
	v_mfma_f32_16x16x32_f16 v[126:129], v[156:159], v[192:195], v[126:129]
	v_mfma_f32_16x16x32_f16 v[122:125], v[164:167], v[192:195], v[122:125]
	v_mfma_f32_16x16x32_f16 v[110:113], v[156:159], v[200:203], v[110:113]
	v_mfma_f32_16x16x32_f16 v[106:109], v[164:167], v[200:203], v[106:109]
	v_mfma_f32_16x16x32_f16 v[94:97], v[156:159], v[208:211], v[94:97]
	v_mfma_f32_16x16x32_f16 v[90:93], v[164:167], v[208:211], v[90:93]
	v_mfma_f32_16x16x32_f16 v[78:81], v[156:159], v[216:219], v[78:81]
	v_mfma_f32_16x16x32_f16 v[74:77], v[164:167], v[216:219], v[74:77]
	s_setprio 0
	s_setprio 1
	v_mfma_f32_16x16x32_f16 v[118:121], v[168:171], v[188:191], v[118:121]
	v_mfma_f32_16x16x32_f16 v[114:117], v[176:179], v[188:191], v[114:117]
	v_mfma_f32_16x16x32_f16 v[102:105], v[168:171], v[196:199], v[102:105]
	v_mfma_f32_16x16x32_f16 v[98:101], v[176:179], v[196:199], v[98:101]
	v_mfma_f32_16x16x32_f16 v[86:89], v[168:171], v[204:207], v[86:89]
	v_mfma_f32_16x16x32_f16 v[82:85], v[176:179], v[204:207], v[82:85]
	v_mfma_f32_16x16x32_f16 v[70:73], v[168:171], v[212:215], v[70:73]
	v_mfma_f32_16x16x32_f16 v[66:69], v[176:179], v[212:215], v[66:69]
	v_mfma_f32_16x16x32_f16 v[118:121], v[172:175], v[192:195], v[118:121]
	v_mfma_f32_16x16x32_f16 v[114:117], v[180:183], v[192:195], v[114:117]
	v_mfma_f32_16x16x32_f16 v[102:105], v[172:175], v[200:203], v[102:105]
	v_mfma_f32_16x16x32_f16 v[98:101], v[180:183], v[200:203], v[98:101]
	v_mfma_f32_16x16x32_f16 v[86:89], v[172:175], v[208:211], v[86:89]
	v_mfma_f32_16x16x32_f16 v[82:85], v[180:183], v[208:211], v[82:85]
	v_mfma_f32_16x16x32_f16 v[70:73], v[172:175], v[216:219], v[70:73]
	v_mfma_f32_16x16x32_f16 v[66:69], v[180:183], v[216:219], v[66:69]
	s_setprio 0
	s_barrier
	s_add_i32 s30, s62, s34
	v_lshl_add_u64 v[184:185], v[184:185], 0, s[12:13]
	s_mov_b32 m0, s30
	ds_read_b128 v[188:191], v154 offset:49152
	ds_read_b128 v[192:195], v154 offset:50176
	ds_read_b128 v[196:199], v154 offset:51200
	ds_read_b128 v[200:203], v154 offset:52224
	ds_read_b128 v[204:207], v154 offset:53248
	ds_read_b128 v[208:211], v154 offset:54272
	ds_read_b128 v[212:215], v154 offset:55296
	ds_read_b128 v[216:219], v154 offset:56320
	global_load_lds_dwordx4 v[184:185], off
	s_add_i32 m0, s30, 0x2000
	s_add_u32 s28, s28, 0x80080
	v_lshl_add_u64 v[184:185], v[220:221], 0, s[12:13]
	s_addc_u32 s29, s29, 0
	s_add_i32 s30, s63, s34
	global_load_lds_dwordx4 v[184:185], off
	v_lshl_add_u64 v[184:185], v[222:223], 0, s[12:13]
	s_mov_b32 m0, s41
	s_nop 0
	global_load_lds_dwordx4 v[184:185], off
	v_lshl_add_u64 v[184:185], v[224:225], 0, s[12:13]
	s_mov_b32 m0, s42
	s_nop 0
	global_load_lds_dwordx4 v[184:185], off
	s_waitcnt vmcnt(4)
	s_waitcnt lgkmcnt(0)
	s_barrier
	s_setprio 1
	s_waitcnt lgkmcnt(0)
	v_mfma_f32_16x16x32_f16 v[62:65], v[146:149], v[188:191], v[62:65]
	v_mfma_f32_16x16x32_f16 v[58:61], v[160:163], v[188:191], v[58:61]
	v_mfma_f32_16x16x32_f16 v[46:49], v[146:149], v[196:199], v[46:49]
	v_mfma_f32_16x16x32_f16 v[42:45], v[160:163], v[196:199], v[42:45]
	v_mfma_f32_16x16x32_f16 v[30:33], v[146:149], v[204:207], v[30:33]
	v_mfma_f32_16x16x32_f16 v[26:29], v[160:163], v[204:207], v[26:29]
	v_mfma_f32_16x16x32_f16 v[14:17], v[146:149], v[212:215], v[14:17]
	v_mfma_f32_16x16x32_f16 v[10:13], v[160:163], v[212:215], v[10:13]
	v_mfma_f32_16x16x32_f16 v[62:65], v[156:159], v[192:195], v[62:65]
	v_mfma_f32_16x16x32_f16 v[58:61], v[164:167], v[192:195], v[58:61]
	v_mfma_f32_16x16x32_f16 v[46:49], v[156:159], v[200:203], v[46:49]
	v_mfma_f32_16x16x32_f16 v[42:45], v[164:167], v[200:203], v[42:45]
	v_mfma_f32_16x16x32_f16 v[30:33], v[156:159], v[208:211], v[30:33]
	v_mfma_f32_16x16x32_f16 v[26:29], v[164:167], v[208:211], v[26:29]
	v_mfma_f32_16x16x32_f16 v[14:17], v[156:159], v[216:219], v[14:17]
	v_mfma_f32_16x16x32_f16 v[10:13], v[164:167], v[216:219], v[10:13]
	s_setprio 0
	s_setprio 1
	v_mfma_f32_16x16x32_f16 v[54:57], v[168:171], v[188:191], v[54:57]
	v_mfma_f32_16x16x32_f16 v[50:53], v[176:179], v[188:191], v[50:53]
	v_mfma_f32_16x16x32_f16 v[38:41], v[168:171], v[196:199], v[38:41]
	v_mfma_f32_16x16x32_f16 v[34:37], v[176:179], v[196:199], v[34:37]
	v_mfma_f32_16x16x32_f16 v[22:25], v[168:171], v[204:207], v[22:25]
	v_mfma_f32_16x16x32_f16 v[18:21], v[176:179], v[204:207], v[18:21]
	v_mfma_f32_16x16x32_f16 v[6:9], v[168:171], v[212:215], v[6:9]
	v_mfma_f32_16x16x32_f16 v[2:5], v[176:179], v[212:215], v[2:5]
	v_mfma_f32_16x16x32_f16 v[54:57], v[172:175], v[192:195], v[54:57]
	v_mfma_f32_16x16x32_f16 v[50:53], v[180:183], v[192:195], v[50:53]
	v_mfma_f32_16x16x32_f16 v[38:41], v[172:175], v[200:203], v[38:41]
	v_mfma_f32_16x16x32_f16 v[34:37], v[180:183], v[200:203], v[34:37]
	v_mfma_f32_16x16x32_f16 v[22:25], v[172:175], v[208:211], v[22:25]
	v_mfma_f32_16x16x32_f16 v[18:21], v[180:183], v[208:211], v[18:21]
	v_mfma_f32_16x16x32_f16 v[6:9], v[172:175], v[216:219], v[6:9]
	v_mfma_f32_16x16x32_f16 v[2:5], v[180:183], v[216:219], v[2:5]
	s_setprio 0
	s_barrier
	s_add_i32 s61, s61, 2
	s_add_u32 s26, s26, 0x100
	s_addc_u32 s27, s27, 0
	s_add_u32 s51, s51, 0x100
	s_addc_u32 s60, s60, 0
	s_cmp_gt_u32 s61, 29
	s_cbranch_scc0 .LBB0_758
	s_and_b64 vcc, exec, s[14:15]
	s_cbranch_vccz .LBB0_761
	s_barrier

	.amdhsa_kernel _Z10hybrid_fwd4Args
		.amdhsa_group_segment_fixed_size 0
		.amdhsa_private_segment_fixed_size 0
		.amdhsa_kernarg_size 552
		.amdhsa_user_sgpr_count 2
		.amdhsa_user_sgpr_dispatch_ptr 0
		.amdhsa_user_sgpr_queue_ptr 0
		.amdhsa_user_sgpr_kernarg_segment_ptr 1
		.amdhsa_user_sgpr_dispatch_id 0
		.amdhsa_user_sgpr_kernarg_preload_length 0
		.amdhsa_user_sgpr_kernarg_preload_offset 0
		.amdhsa_user_sgpr_private_segment_size 0
		.amdhsa_uses_dynamic_stack 0
		.amdhsa_enable_private_segment 0
		.amdhsa_system_sgpr_workgroup_id_x 1
		.amdhsa_system_sgpr_workgroup_id_y 0
		.amdhsa_system_sgpr_workgroup_id_z 0
		.amdhsa_system_sgpr_workgroup_info 0
		.amdhsa_system_vgpr_workitem_id 0
		.amdhsa_next_free_vgpr 240
		.amdhsa_next_free_sgpr 102
		.amdhsa_accum_offset 240
		.amdhsa_reserve_vcc 1
		.amdhsa_float_round_mode_32 0
		.amdhsa_float_round_mode_16_64 0
		.amdhsa_float_denorm_mode_32 3
		.amdhsa_float_denorm_mode_16_64 3
		.amdhsa_dx10_clamp 1
		.amdhsa_ieee_mode 1
		.amdhsa_fp16_overflow 0
		.amdhsa_tg_split 0
		.amdhsa_exception_fp_ieee_invalid_op 0
		.amdhsa_exception_fp_denorm_src 0
		.amdhsa_exception_fp_ieee_div_zero 0
		.amdhsa_exception_fp_ieee_overflow 0
		.amdhsa_exception_fp_ieee_underflow 0
		.amdhsa_exception_fp_ieee_inexact 0
		.amdhsa_exception_int_div_zero 0
	.end_amdhsa_kernel

amdhsa.kernels:
  - .agpr_count:     0
    .args:
      - .offset:         0
        .size:           296
        .value_kind:     by_value
      - .offset:         296
        .size:           4
        .value_kind:     hidden_block_count_x
      - .offset:         300
        .size:           4
        .value_kind:     hidden_block_count_y
      - .offset:         304
        .size:           4
        .value_kind:     hidden_block_count_z
      - .offset:         308
        .size:           2
        .value_kind:     hidden_group_size_x
      - .offset:         310
        .size:           2
        .value_kind:     hidden_group_size_y
      - .offset:         312
        .size:           2
        .value_kind:     hidden_group_size_z
      - .offset:         314
        .size:           2
        .value_kind:     hidden_remainder_x
      - .offset:         316
        .size:           2
        .value_kind:     hidden_remainder_y
      - .offset:         318
        .size:           2
        .value_kind:     hidden_remainder_z
      - .offset:         336
        .size:           8
        .value_kind:     hidden_global_offset_x
      - .offset:         344
        .size:           8
        .value_kind:     hidden_global_offset_y
      - .offset:         352
        .size:           8
        .value_kind:     hidden_global_offset_z
      - .offset:         360
        .size:           2
        .value_kind:     hidden_grid_dims
      - .offset:         416
        .size:           4
        .value_kind:     hidden_dynamic_lds_size
    .group_segment_fixed_size: 0
    .kernarg_segment_align: 8
    .kernarg_segment_size: 552
    .language:       OpenCL C
    .language_version:
      - 2
      - 0
    .max_flat_workgroup_size: 512
    .name:           _Z10hybrid_fwd4Args
    .private_segment_fixed_size: 0
    .sgpr_count:     108
    .sgpr_spill_count: 89
    .symbol:         _Z10hybrid_fwd4Args.kd
    .uniform_work_group_size: 1
    .uses_dynamic_stack: false
    .vgpr_count:     240
    .vgpr_spill_count: 0
    .wavefront_size: 64
